# v17: scan y tile stored as one 8-byte write-through store per lane per chunk (quad transpose by DPP + v_perm)
# baseline (speedup 1.0000x reference)
.LBB0_1721:
	s_and_b32 s56, s83, 31
	s_bfe_u32 s73, s83, 0x10005
	s_lshl_b32 s72, s56, 6
	s_cmp_lt_u32 s83, 64
	s_cselect_b64 s[28:29], -1, 0
	s_and_b64 s[66:67], s[28:29], exec
	s_mov_b32 s0, 0x8c00000
	s_cselect_b32 s0, s0, 0x29400000
	s_add_u32 s66, s54, s0
	s_addc_u32 s67, s55, 0
	s_andn2_b64 vcc, exec, s[50:51]
	s_mov_b64 s[68:69], -1
	s_cbranch_vccnz .LBB0_1737
	s_setprio 1
	s_and_saveexec_b64 s[68:69], s[4:5]
	v_mov_b32_e32 v2, s61
	ds_write_b32 v2, v161
	s_or_b64 exec, exec, s[68:69]
	s_lshl_b32 s0, s72, 1
	s_add_u32 s0, s66, s0
	s_addc_u32 s1, s67, 0
	s_add_u32 s0, s0, s81
	s_addc_u32 s1, s1, 0
	v_lshlrev_b32_e32 v160, 1, v158
	v_mov_b32_e32 v2, 0
	v_lshl_add_u64 v[164:165], s[0:1], 0, v[160:161]
	s_lshl_b32 s70, s73, 14
	s_mov_b32 s71, 0
	v_mov_b32_e32 v3, v2
	v_mov_b32_e32 v4, v2
	v_mov_b32_e32 v5, v2
	v_mov_b32_e32 v10, v2
	v_mov_b32_e32 v11, v2
	v_mov_b32_e32 v12, v2
	v_mov_b32_e32 v13, v2
	v_mov_b32_e32 v6, v2
	v_mov_b32_e32 v7, v2
	v_mov_b32_e32 v8, v2
	v_mov_b32_e32 v9, v2
	v_mov_b32_e32 v14, v2
	v_mov_b32_e32 v15, v2
	v_mov_b32_e32 v16, v2
	v_mov_b32_e32 v17, v2
	v_and_b32_e32 v25, 3, v0
	v_add_u32_e32 v24, v184, v25
	v_add_u32_e32 v22, 0xffffff00, v24
	v_sub_u32_e32 v23, 0x40ff, v24
	v_cndmask_b32_e64 v22, v23, v22, s[28:29]
	v_add_u32_e32 v22, s70, v22
	v_ashrrev_i32_e32 v23, 31, v22
	v_lshlrev_b64 v[22:23], 12, v[22:23]
	v_lshl_add_u64 v[22:23], v[164:165], 0, v[22:23]
	v_sub_u32_e32 v27, 0, v25
	v_lshlrev_b32_e32 v26, 1, v27
	v_ashrrev_i32_e32 v27, 31, v26
	v_lshl_add_u64 v[210:211], v[22:23], 0, v[26:27]
	v_and_b32_e32 v25, 1, v0
	v_cmp_ne_u32_e32 vcc, 0, v25
	v_mov_b32_e32 v28, 0x05040100
	v_mov_b32_e32 v29, 0x03020706
	v_cndmask_b32_e32 v212, v28, v29, vcc
	s_mov_b32 s100, 0x10000
	s_mov_b32 s101, 0
	s_cmp_lt_u32 s83, 64
	s_cbranch_scc1 .Lx14_dir0
	s_mov_b32 s100, 0xffff0000
	s_mov_b32 s101, -1

.LBB0_1725:
	s_cmp_eq_u32 s82, 0
	s_cbranch_scc1 .Lx14_w0
	s_waitcnt vmcnt(4)
	s_branch .Lx14_wj
.Lx14_w0:
	s_waitcnt vmcnt(5)

.LBB0_1731:
	v_lshl_add_u64 v[210:211], v[210:211], 0, s[100:101]
	s_add_i32 s69, s69, 1
	s_cmp_eq_u32 s69, 4
	s_cbranch_scc1 .LBB0_1725

.LBB0_1734:
	s_mul_i32 s0, s69, 0x3300
	s_add_i32 s0, s74, s0
	s_add_i32 s1, s0, 0x2a00
	v_add_u32_e32 v18, s1, v185
	ds_read_b64_tr_b16 v[20:21], v18
	v_add3_u32 v18, s0, v186, v187
	ds_read2_b64 v[26:29], v18 offset1:4
	ds_read2_b64 v[30:33], v18 offset0:8 offset1:12
	v_add_u32_e32 v18, 0x800, v18
	v_cvt_pk_bf16_f32 v22, v2, v3
	v_cvt_pk_bf16_f32 v23, v4, v5
	v_cvt_pk_bf16_f32 v24, v10, v11
	v_cvt_pk_bf16_f32 v25, v12, v13
	ds_read2_b64 v[38:41], v18 offset0:32 offset1:36
	ds_read2_b64 v[42:45], v18 offset0:40 offset1:44
	s_waitcnt lgkmcnt(3)
	v_mfma_f32_16x16x32_bf16 v[26:29], v[26:29], v[22:25], 0
	s_waitcnt lgkmcnt(0)
	s_add_i32 s76, s69, s68
	v_cvt_pk_bf16_f32 v34, v6, v7
	v_cvt_pk_bf16_f32 v35, v8, v9
	v_cvt_pk_bf16_f32 v36, v14, v15
	v_cvt_pk_bf16_f32 v37, v16, v17
	s_waitcnt lgkmcnt(2)
	s_nop 0
	v_mfma_f32_16x16x32_bf16 v[26:29], v[30:33], v[34:37], v[26:29]
	s_nop 7
	v_cvt_pk_bf16_f32 v18, v26, v27
	v_add_u32_e32 v26, s0, v192
	ds_read_b128 v[30:33], v26 offset:8704
	v_add_u32_e32 v62, s0, v191
	ds_read_b128 v[46:49], v62 offset:12800
	v_cvt_pk_bf16_f32 v19, v28, v29
	ds_read_b128 v[26:29], v26 offset:9728
	ds_read_b128 v[50:53], v62 offset:12864
	v_add_u32_e32 v63, v62, v190
	ds_read_b128 v[54:57], v63 offset:4608
	ds_read_b128 v[58:61], v63 offset:5632
	s_waitcnt lgkmcnt(5)
	v_mfma_f32_16x16x32_bf16 v[30:33], v[30:33], v[18:21], 0
	s_waitcnt lgkmcnt(2)
	v_pk_mul_f32 v[10:11], v[10:11], v[50:51]
	v_pk_mul_f32 v[12:13], v[12:13], v[52:53]
	ds_read_b128 v[50:53], v63 offset:7680
	v_mfma_f32_16x16x32_bf16 v[22:25], v[38:41], v[22:25], 0
	s_nop 2
	v_cvt_pk_bf16_f32 v18, v30, v31
	v_cvt_pk_bf16_f32 v19, v32, v33
	ds_read_b128 v[30:33], v63 offset:6656
	v_pk_mul_f32 v[2:3], v[2:3], v[46:47]
	v_pk_mul_f32 v[4:5], v[4:5], v[48:49]
	ds_read_b128 v[46:49], v62 offset:12928
	v_mfma_f32_16x16x32_bf16 v[22:25], v[42:45], v[34:37], v[22:25]
	s_cmp_lt_u32 s76, 16
	s_waitcnt lgkmcnt(4)
	v_mfma_f32_16x16x32_bf16 v[2:5], v[54:57], v[18:21], v[2:5]
	ds_read_b128 v[54:57], v62 offset:12992
	s_waitcnt lgkmcnt(1)
	v_pk_mul_f32 v[6:7], v[6:7], v[46:47]
	v_pk_mul_f32 v[8:9], v[8:9], v[48:49]
	v_mfma_f32_16x16x32_bf16 v[10:13], v[58:61], v[18:21], v[10:13]
	s_waitcnt lgkmcnt(0)
	v_pk_mul_f32 v[14:15], v[14:15], v[54:55]
	v_pk_mul_f32 v[16:17], v[16:17], v[56:57]
	v_mfma_f32_16x16x32_bf16 v[6:9], v[30:33], v[18:21], v[6:9]
	s_nop 0
	v_mfma_f32_16x16x32_bf16 v[14:17], v[50:53], v[18:21], v[14:17]
	v_mfma_f32_16x16x32_bf16 v[18:21], v[26:29], v[18:21], v[22:25]
	s_cbranch_scc1 .LBB0_1731
	s_nop 6
	v_cvt_pk_bf16_f32 v32, v18, v19
	v_cvt_pk_bf16_f32 v33, v20, v21
	v_and_b32_e32 v25, 2, v0
	v_cmp_ne_u32_e32 vcc, 0, v25
	v_mov_b32_dpp v34, v32 quad_perm:[1,0,3,2] row_mask:0xf bank_mask:0xf bound_ctrl:1
	v_mov_b32_dpp v35, v33 quad_perm:[1,0,3,2] row_mask:0xf bank_mask:0xf bound_ctrl:1
	v_perm_b32 v36, v34, v32, v212
	v_perm_b32 v37, v35, v33, v212
	v_cndmask_b32_e32 v38, v36, v37, vcc
	v_cndmask_b32_e32 v39, v37, v36, vcc
	s_nop 1
	v_mov_b32_dpp v40, v39 quad_perm:[2,3,0,1] row_mask:0xf bank_mask:0xf bound_ctrl:1
	v_cndmask_b32_e32 v36, v38, v40, vcc
	v_cndmask_b32_e32 v37, v40, v38, vcc
	global_store_dwordx2 v[210:211], v[36:37], off sc1
	s_branch .LBB0_1731
